# removed the three explicit s_nop 15 x2 MFMA->VALU pads at the fp8 epilogue starts (real dependency distance is far larger) on top of v62
# baseline (speedup 1.0000x reference)
.LBB0_541:
	s_mul_hi_u32 s2, s7, 0xaaaaaaab
	s_lshr_b32 s2, s2, 1
	s_mul_i32 s2, s2, 3
	s_sub_i32 s2, s7, s2
	s_lshl_b32 s3, s2, 10
	s_lshl_b32 s2, s22, 1
	v_add_u32_e32 v168, s3, v171
	s_add_i32 s3, s2, -15
	s_cmp_lt_u32 s3, 3
	ds_read_b128 v[4:7], v168
	ds_read_b128 v[0:3], v168 offset:16
	s_cselect_b64 s[24:25], -1, 0
	s_add_i32 s7, s2, -3
	s_cmp_lt_u32 s7, 3
	s_cselect_b64 vcc, -1, 0
	v_mov_b32_e32 v8, 0x3b5105ec
	v_cndmask_b32_e32 v24, v200, v8, vcc
	s_cmp_gt_u32 s3, 2
	s_waitcnt lgkmcnt(0)
	v_pk_fma_f32 v[8:9], v[24:25], v[156:157], v[4:5] op_sel_hi:[0,1,1]
	v_pk_fma_f32 v[10:11], v[24:25], v[158:159], v[6:7] op_sel_hi:[0,1,1]
	v_pk_fma_f32 v[12:13], v[24:25], v[152:153], v[0:1] op_sel_hi:[0,1,1]
	v_pk_fma_f32 v[14:15], v[24:25], v[154:155], v[2:3] op_sel_hi:[0,1,1]
	s_cbranch_scc1 .LBB0_543
	v_pk_mul_f32 v[16:17], v[10:11], v[10:11]
	v_pk_mul_f32 v[18:19], v[8:9], v[8:9]
	v_pk_mul_f32 v[20:21], v[14:15], v[14:15]
	v_pk_mul_f32 v[22:23], v[12:13], v[12:13]
	v_pk_mul_f32 v[16:17], v[10:11], v[16:17]
	v_pk_mul_f32 v[18:19], v[8:9], v[18:19]
	v_pk_mul_f32 v[20:21], v[14:15], v[20:21]
	v_pk_mul_f32 v[22:23], v[12:13], v[22:23]
	v_pk_fma_f32 v[18:19], v[18:19], s[42:43], v[8:9] op_sel_hi:[1,0,1]
	v_pk_fma_f32 v[16:17], v[16:17], s[42:43], v[10:11] op_sel_hi:[1,0,1]
	v_pk_fma_f32 v[22:23], v[22:23], s[42:43], v[12:13] op_sel_hi:[1,0,1]
	v_pk_fma_f32 v[20:21], v[20:21], s[42:43], v[14:15] op_sel_hi:[1,0,1]
	v_pk_mul_f32 v[18:19], v[18:19], s[96:97] op_sel_hi:[1,0]
	v_pk_mul_f32 v[16:17], v[16:17], s[96:97] op_sel_hi:[1,0]
	v_pk_mul_f32 v[22:23], v[22:23], s[96:97] op_sel_hi:[1,0]
	v_pk_mul_f32 v[20:21], v[20:21], s[96:97] op_sel_hi:[1,0]
	v_exp_f32_e32 v18, v18
	v_exp_f32_e32 v19, v19
	v_exp_f32_e32 v16, v16
	v_exp_f32_e32 v17, v17
	v_exp_f32_e32 v22, v22
	v_exp_f32_e32 v23, v23
	v_exp_f32_e32 v20, v20
	v_exp_f32_e32 v21, v21
	v_pk_add_f32 v[18:19], v[18:19], 1.0 op_sel_hi:[1,0]
	v_pk_add_f32 v[16:17], v[16:17], 1.0 op_sel_hi:[1,0]
	v_pk_add_f32 v[22:23], v[22:23], 1.0 op_sel_hi:[1,0]
	v_pk_add_f32 v[20:21], v[20:21], 1.0 op_sel_hi:[1,0]
	v_rcp_f32_e32 v18, v18
	v_rcp_f32_e32 v19, v19
	v_rcp_f32_e32 v16, v16
	v_rcp_f32_e32 v17, v17
	v_rcp_f32_e32 v22, v22
	v_rcp_f32_e32 v23, v23
	v_rcp_f32_e32 v20, v20
	v_rcp_f32_e32 v21, v21
	v_pk_mul_f32 v[8:9], v[8:9], v[18:19]
	v_pk_mul_f32 v[10:11], v[10:11], v[16:17]
	v_pk_mul_f32 v[12:13], v[12:13], v[22:23]
	v_pk_mul_f32 v[14:15], v[14:15], v[20:21]

.LBB0_1540:
	s_mul_hi_u32 s2, s57, 0xaaaaaaab
	s_lshr_b32 s2, s2, 1
	s_mul_i32 s2, s2, 3
	s_sub_i32 s2, s57, s2
	v_lshl_add_u32 v6, s2, 10, v195
	ds_read_b128 v[12:15], v6
	ds_read_b128 v[0:3], v6 offset:16
	ds_read_b128 v[8:11], v6 offset:512
	v_readlane_b32 s2, v253, 54
	s_waitcnt lgkmcnt(0)
	v_pk_fma_f32 v[4:5], v[156:157], s[38:39], v[12:13] op_sel_hi:[1,0,1]
	v_pk_fma_f32 v[22:23], v[152:153], s[38:39], v[8:9] op_sel_hi:[1,0,1]
	v_min_f32_e32 v17, 0x40e00000, v5
	v_min_f32_e32 v16, 0x40e00000, v4
	v_pk_mul_f32 v[4:5], v[16:17], s[88:89] op_sel_hi:[1,0]
	v_med3_f32 v23, v23, s55, v213
	v_exp_f32_e32 v20, v4
	v_exp_f32_e32 v21, v5
	v_med3_f32 v22, v22, s55, v213
	v_pk_add_f32 v[22:23], v[22:23], 1.0 op_sel_hi:[1,0]
	v_pk_fma_f32 v[24:25], v[154:155], s[38:39], v[10:11] op_sel_hi:[1,0,1]
	v_pk_add_f32 v[20:21], v[20:21], 1.0 op_sel_hi:[1,0]
	v_pk_mul_f32 v[16:17], v[16:17], v[22:23]
	v_rcp_f32_e32 v20, v20
	v_rcp_f32_e32 v21, v21
	v_med3_f32 v25, v25, s55, v213
	v_med3_f32 v24, v24, s55, v213
	v_pk_add_f32 v[24:25], v[24:25], 1.0 op_sel_hi:[1,0]
	v_pk_mul_f32 v[16:17], v[16:17], v[20:21]
	v_pk_fma_f32 v[20:21], v[158:159], s[38:39], v[14:15] op_sel_hi:[1,0,1]
	ds_read_b128 v[4:7], v6 offset:528
	v_min_f32_e32 v21, 0x40e00000, v21
	v_min_f32_e32 v20, 0x40e00000, v20
	v_pk_mul_f32 v[22:23], v[20:21], s[88:89] op_sel_hi:[1,0]
	v_pk_mul_f32 v[20:21], v[20:21], v[24:25]
	v_exp_f32_e32 v22, v22
	v_exp_f32_e32 v23, v23
	v_pk_fma_f32 v[24:25], v[148:149], s[38:39], v[0:1] op_sel_hi:[1,0,1]
	s_waitcnt lgkmcnt(0)
	v_pk_fma_f32 v[28:29], v[146:147], s[38:39], v[6:7] op_sel_hi:[1,0,1]
	v_min_f32_e32 v25, 0x40e00000, v25
	v_min_f32_e32 v24, 0x40e00000, v24
	v_pk_add_f32 v[22:23], v[22:23], 1.0 op_sel_hi:[1,0]
	v_pk_mul_f32 v[26:27], v[24:25], s[88:89] op_sel_hi:[1,0]
	v_rcp_f32_e32 v22, v22
	v_rcp_f32_e32 v23, v23
	v_exp_f32_e32 v26, v26
	v_exp_f32_e32 v27, v27
	v_med3_f32 v29, v29, s55, v213
	v_pk_mul_f32 v[20:21], v[20:21], v[22:23]
	v_pk_fma_f32 v[22:23], v[144:145], s[38:39], v[4:5] op_sel_hi:[1,0,1]
	v_pk_add_f32 v[26:27], v[26:27], 1.0 op_sel_hi:[1,0]
	v_med3_f32 v23, v23, s55, v213
	v_rcp_f32_e32 v26, v26
	v_rcp_f32_e32 v27, v27
	v_med3_f32 v22, v22, s55, v213
	v_pk_add_f32 v[22:23], v[22:23], 1.0 op_sel_hi:[1,0]
	v_med3_f32 v28, v28, s55, v213
	v_pk_mul_f32 v[22:23], v[24:25], v[22:23]
	v_pk_fma_f32 v[24:25], v[150:151], s[38:39], v[2:3] op_sel_hi:[1,0,1]
	v_pk_mul_f32 v[22:23], v[22:23], v[26:27]
	v_min_f32_e32 v25, 0x40e00000, v25
	v_min_f32_e32 v24, 0x40e00000, v24
	v_pk_mul_f32 v[26:27], v[24:25], s[88:89] op_sel_hi:[1,0]
	v_pk_add_f32 v[28:29], v[28:29], 1.0 op_sel_hi:[1,0]
	v_exp_f32_e32 v26, v26
	v_exp_f32_e32 v27, v27
	v_cvt_pk_fp8_f32 v30, v16, v17
	v_pk_mul_f32 v[16:17], v[24:25], v[28:29]
	v_pk_fma_f32 v[24:25], v[140:141], s[38:39], v[12:13] op_sel_hi:[1,0,1]
	v_pk_add_f32 v[26:27], v[26:27], 1.0 op_sel_hi:[1,0]
	v_min_f32_e32 v25, 0x40e00000, v25
	v_rcp_f32_e32 v26, v26
	v_rcp_f32_e32 v27, v27
	v_min_f32_e32 v24, 0x40e00000, v24
	v_cvt_pk_fp8_f32 v31, v22, v23
	v_pk_fma_f32 v[28:29], v[136:137], s[38:39], v[8:9] op_sel_hi:[1,0,1]
	v_pk_mul_f32 v[16:17], v[16:17], v[26:27]
	v_pk_mul_f32 v[26:27], v[24:25], s[88:89] op_sel_hi:[1,0]
	v_med3_f32 v29, v29, s55, v213
	v_exp_f32_e32 v26, v26
	v_exp_f32_e32 v27, v27
	v_med3_f32 v28, v28, s55, v213
	v_cvt_pk_fp8_f32 v30, v20, v21 op_sel:[0,0,1]
	v_cvt_pk_fp8_f32 v31, v16, v17 op_sel:[0,0,1]
	v_pk_add_f32 v[26:27], v[26:27], 1.0 op_sel_hi:[1,0]
	v_pk_add_f32 v[28:29], v[28:29], 1.0 op_sel_hi:[1,0]
	v_rcp_f32_e32 v26, v26
	v_rcp_f32_e32 v27, v27
	v_pk_mul_f32 v[24:25], v[24:25], v[28:29]
	ds_bpermute_b32 v22, v167, v30
	ds_bpermute_b32 v23, v167, v31
	v_pk_mul_f32 v[24:25], v[24:25], v[26:27]
	v_pk_fma_f32 v[26:27], v[142:143], s[38:39], v[14:15] op_sel_hi:[1,0,1]
	v_pk_fma_f32 v[30:31], v[138:139], s[38:39], v[10:11] op_sel_hi:[1,0,1]
	v_min_f32_e32 v27, 0x40e00000, v27
	v_min_f32_e32 v26, 0x40e00000, v26
	v_pk_mul_f32 v[28:29], v[26:27], s[88:89] op_sel_hi:[1,0]
	v_med3_f32 v31, v31, s55, v213
	v_exp_f32_e32 v28, v28
	v_exp_f32_e32 v29, v29
	v_med3_f32 v30, v30, s55, v213
	v_pk_add_f32 v[30:31], v[30:31], 1.0 op_sel_hi:[1,0]
	v_lshl_add_u32 v20, v219, 8, v171
	v_pk_mul_f32 v[26:27], v[26:27], v[30:31]
	v_pk_fma_f32 v[30:31], v[132:133], s[38:39], v[0:1] op_sel_hi:[1,0,1]
	v_pk_add_f32 v[28:29], v[28:29], 1.0 op_sel_hi:[1,0]
	v_min_f32_e32 v31, 0x40e00000, v31
	v_min_f32_e32 v30, 0x40e00000, v30
	v_pk_mul_f32 v[132:133], v[30:31], s[88:89] op_sel_hi:[1,0]
	v_rcp_f32_e32 v28, v28
	v_rcp_f32_e32 v29, v29
	v_exp_f32_e32 v132, v132
	v_exp_f32_e32 v133, v133
	v_ashrrev_i32_e32 v21, 31, v20
	v_lshlrev_b64 v[16:17], 10, v[20:21]
	v_pk_mul_f32 v[26:27], v[26:27], v[28:29]
	v_pk_fma_f32 v[28:29], v[128:129], s[38:39], v[4:5] op_sel_hi:[1,0,1]
	v_pk_add_f32 v[128:129], v[132:133], 1.0 op_sel_hi:[1,0]
	v_cvt_pk_fp8_f32 v21, v24, v25
	v_rcp_f32_e32 v128, v128
	v_rcp_f32_e32 v129, v129
	v_med3_f32 v29, v29, s55, v213
	v_med3_f32 v28, v28, s55, v213
	v_pk_add_f32 v[28:29], v[28:29], 1.0 op_sel_hi:[1,0]
	v_cvt_pk_fp8_f32 v21, v26, v27 op_sel:[0,0,1]
	v_pk_mul_f32 v[28:29], v[30:31], v[28:29]
	v_pk_fma_f32 v[26:27], v[124:125], s[38:39], v[12:13] op_sel_hi:[1,0,1]
	v_pk_mul_f32 v[28:29], v[28:29], v[128:129]
	v_mov_b32_e32 v132, v173
	v_min_f32_e32 v27, 0x40e00000, v27
	v_min_f32_e32 v26, 0x40e00000, v26
	v_cvt_pk_fp8_f32 v132, v28, v29
	v_pk_mul_f32 v[28:29], v[26:27], s[88:89] op_sel_hi:[1,0]
	v_pk_fma_f32 v[130:131], v[130:131], s[38:39], v[6:7] op_sel_hi:[1,0,1]
	v_exp_f32_e32 v28, v28
	v_exp_f32_e32 v29, v29
	v_pk_fma_f32 v[30:31], v[134:135], s[38:39], v[2:3] op_sel_hi:[1,0,1]
	v_med3_f32 v131, v131, s55, v213
	v_med3_f32 v130, v130, s55, v213
	v_min_f32_e32 v31, 0x40e00000, v31
	v_min_f32_e32 v30, 0x40e00000, v30
	v_pk_add_f32 v[130:131], v[130:131], 1.0 op_sel_hi:[1,0]
	v_pk_add_f32 v[28:29], v[28:29], 1.0 op_sel_hi:[1,0]
	v_pk_mul_f32 v[128:129], v[30:31], s[88:89] op_sel_hi:[1,0]
	v_pk_mul_f32 v[24:25], v[30:31], v[130:131]
	v_pk_fma_f32 v[30:31], v[120:121], s[38:39], v[8:9] op_sel_hi:[1,0,1]
	v_rcp_f32_e32 v28, v28
	v_rcp_f32_e32 v29, v29
	v_med3_f32 v31, v31, s55, v213
	v_med3_f32 v30, v30, s55, v213
	v_pk_add_f32 v[30:31], v[30:31], 1.0 op_sel_hi:[1,0]
	v_pk_fma_f32 v[120:121], v[122:123], s[38:39], v[10:11] op_sel_hi:[1,0,1]
	v_pk_mul_f32 v[26:27], v[26:27], v[30:31]
	v_med3_f32 v121, v121, s55, v213
	v_pk_mul_f32 v[26:27], v[26:27], v[28:29]
	v_pk_fma_f32 v[28:29], v[126:127], s[38:39], v[14:15] op_sel_hi:[1,0,1]
	v_med3_f32 v120, v120, s55, v213
	v_min_f32_e32 v29, 0x40e00000, v29
	v_min_f32_e32 v28, 0x40e00000, v28
	v_pk_mul_f32 v[30:31], v[28:29], s[88:89] op_sel_hi:[1,0]
	v_pk_fma_f32 v[116:117], v[116:117], s[38:39], v[0:1] op_sel_hi:[1,0,1]
	v_exp_f32_e32 v30, v30
	v_exp_f32_e32 v31, v31
	v_pk_add_f32 v[120:121], v[120:121], 1.0 op_sel_hi:[1,0]
	v_min_f32_e32 v117, 0x40e00000, v117
	v_min_f32_e32 v116, 0x40e00000, v116
	v_pk_add_f32 v[30:31], v[30:31], 1.0 op_sel_hi:[1,0]
	v_pk_mul_f32 v[28:29], v[28:29], v[120:121]
	v_pk_mul_f32 v[120:121], v[116:117], s[88:89] op_sel_hi:[1,0]
	v_rcp_f32_e32 v30, v30
	v_rcp_f32_e32 v31, v31
	v_exp_f32_e32 v120, v120
	v_exp_f32_e32 v121, v121
	v_lshl_or_b32 v18, v220, 7, v194
	v_pk_mul_f32 v[28:29], v[28:29], v[30:31]
	v_pk_fma_f32 v[30:31], v[112:113], s[38:39], v[4:5] op_sel_hi:[1,0,1]
	v_pk_add_f32 v[112:113], v[120:121], 1.0 op_sel_hi:[1,0]
	v_med3_f32 v31, v31, s55, v213
	v_rcp_f32_e32 v112, v112
	v_rcp_f32_e32 v113, v113
	v_med3_f32 v30, v30, s55, v213
	v_pk_add_f32 v[30:31], v[30:31], 1.0 op_sel_hi:[1,0]
	v_readlane_b32 s3, v253, 55
	v_pk_mul_f32 v[30:31], v[116:117], v[30:31]
	v_ashrrev_i32_e32 v19, 31, v18
	v_pk_mul_f32 v[30:31], v[30:31], v[112:113]
	v_pk_fma_f32 v[112:113], v[118:119], s[38:39], v[2:3] op_sel_hi:[1,0,1]
	v_lshl_add_u64 v[16:17], s[2:3], 0, v[16:17]
	v_min_f32_e32 v113, 0x40e00000, v113
	v_min_f32_e32 v112, 0x40e00000, v112
	v_pk_mul_f32 v[116:117], v[112:113], s[88:89] op_sel_hi:[1,0]
	v_pk_fma_f32 v[114:115], v[114:115], s[38:39], v[6:7] op_sel_hi:[1,0,1]
	v_exp_f32_e32 v116, v116
	v_exp_f32_e32 v117, v117
	v_lshl_add_u64 v[16:17], v[16:17], 0, v[18:19]
	v_med3_f32 v115, v115, s55, v213
	v_pk_add_f32 v[116:117], v[116:117], 1.0 op_sel_hi:[1,0]
	v_med3_f32 v114, v114, s55, v213
	v_rcp_f32_e32 v116, v116
	v_rcp_f32_e32 v117, v117
	v_cvt_pk_fp8_f32 v118, v30, v31
	s_waitcnt lgkmcnt(0)
	global_store_dwordx2 v[16:17], v[22:23], off
	ds_bpermute_b32 v22, v167, v21
	v_pk_add_f32 v[114:115], v[114:115], 1.0 op_sel_hi:[1,0]
	v_cvt_pk_fp8_f32 v21, v26, v27
	v_pk_mul_f32 v[26:27], v[112:113], v[114:115]
	v_pk_fma_f32 v[30:31], v[104:105], s[38:39], v[8:9] op_sel_hi:[1,0,1]
	v_pk_mul_f32 v[26:27], v[26:27], v[116:117]
	v_cvt_pk_fp8_f32 v21, v28, v29 op_sel:[0,0,1]
	v_cvt_pk_fp8_f32 v118, v26, v27 op_sel:[0,0,1]
	v_pk_fma_f32 v[26:27], v[108:109], s[38:39], v[12:13] op_sel_hi:[1,0,1]
	v_med3_f32 v31, v31, s55, v213
	v_min_f32_e32 v27, 0x40e00000, v27
	v_min_f32_e32 v26, 0x40e00000, v26
	v_pk_mul_f32 v[28:29], v[26:27], s[88:89] op_sel_hi:[1,0]
	v_med3_f32 v30, v30, s55, v213
	v_exp_f32_e32 v28, v28
	v_exp_f32_e32 v29, v29
	v_pk_add_f32 v[30:31], v[30:31], 1.0 op_sel_hi:[1,0]
	v_exp_f32_e32 v128, v128
	v_pk_mul_f32 v[26:27], v[26:27], v[30:31]
	v_pk_add_f32 v[28:29], v[28:29], 1.0 op_sel_hi:[1,0]
	v_exp_f32_e32 v129, v129
	v_rcp_f32_e32 v28, v28
	v_rcp_f32_e32 v29, v29
	v_pk_fma_f32 v[104:105], v[106:107], s[38:39], v[10:11] op_sel_hi:[1,0,1]
	v_pk_add_f32 v[128:129], v[128:129], 1.0 op_sel_hi:[1,0]
	v_med3_f32 v105, v105, s55, v213
	v_pk_mul_f32 v[26:27], v[26:27], v[28:29]
	v_pk_fma_f32 v[28:29], v[110:111], s[38:39], v[14:15] op_sel_hi:[1,0,1]
	v_med3_f32 v104, v104, s55, v213
	v_min_f32_e32 v29, 0x40e00000, v29
	v_min_f32_e32 v28, 0x40e00000, v28
	v_pk_mul_f32 v[30:31], v[28:29], s[88:89] op_sel_hi:[1,0]
	v_pk_fma_f32 v[100:101], v[100:101], s[38:39], v[0:1] op_sel_hi:[1,0,1]
	v_exp_f32_e32 v30, v30
	v_exp_f32_e32 v31, v31
	v_rcp_f32_e32 v128, v128
	v_rcp_f32_e32 v129, v129
	v_pk_add_f32 v[104:105], v[104:105], 1.0 op_sel_hi:[1,0]
	v_min_f32_e32 v101, 0x40e00000, v101
	v_min_f32_e32 v100, 0x40e00000, v100
	v_pk_add_f32 v[30:31], v[30:31], 1.0 op_sel_hi:[1,0]
	v_pk_mul_f32 v[28:29], v[28:29], v[104:105]
	v_pk_mul_f32 v[104:105], v[100:101], s[88:89] op_sel_hi:[1,0]
	v_rcp_f32_e32 v30, v30
	v_rcp_f32_e32 v31, v31
	v_exp_f32_e32 v104, v104
	v_exp_f32_e32 v105, v105
	v_pk_mul_f32 v[24:25], v[24:25], v[128:129]
	v_pk_mul_f32 v[28:29], v[28:29], v[30:31]
	v_cvt_pk_fp8_f32 v132, v24, v25 op_sel:[0,0,1]
	v_pk_fma_f32 v[30:31], v[96:97], s[38:39], v[4:5] op_sel_hi:[1,0,1]
	v_pk_add_f32 v[96:97], v[104:105], 1.0 op_sel_hi:[1,0]
	v_med3_f32 v31, v31, s55, v213
	v_rcp_f32_e32 v96, v96
	v_rcp_f32_e32 v97, v97
	v_med3_f32 v30, v30, s55, v213
	ds_bpermute_b32 v23, v167, v132
	v_or_b32_e32 v24, 16, v20
	v_pk_add_f32 v[30:31], v[30:31], 1.0 op_sel_hi:[1,0]
	v_ashrrev_i32_e32 v25, 31, v24
	v_pk_mul_f32 v[30:31], v[100:101], v[30:31]
	v_lshlrev_b64 v[24:25], 10, v[24:25]
	v_pk_mul_f32 v[30:31], v[30:31], v[96:97]
	v_pk_fma_f32 v[96:97], v[102:103], s[38:39], v[2:3] op_sel_hi:[1,0,1]
	v_lshl_add_u64 v[24:25], s[2:3], 0, v[24:25]
	v_min_f32_e32 v97, 0x40e00000, v97
	v_min_f32_e32 v96, 0x40e00000, v96
	v_lshl_add_u64 v[24:25], v[24:25], 0, v[18:19]
	v_pk_mul_f32 v[100:101], v[96:97], s[88:89] op_sel_hi:[1,0]
	s_waitcnt lgkmcnt(0)
	global_store_dwordx2 v[24:25], v[22:23], off
	ds_bpermute_b32 v22, v167, v21
	v_exp_f32_e32 v100, v100
	v_exp_f32_e32 v101, v101
	v_cvt_pk_fp8_f32 v21, v26, v27
	ds_bpermute_b32 v23, v167, v118
	v_or_b32_e32 v24, 32, v20
	v_pk_add_f32 v[100:101], v[100:101], 1.0 op_sel_hi:[1,0]
	v_ashrrev_i32_e32 v25, 31, v24
	v_pk_fma_f32 v[98:99], v[98:99], s[38:39], v[6:7] op_sel_hi:[1,0,1]
	v_rcp_f32_e32 v100, v100
	v_rcp_f32_e32 v101, v101
	v_cvt_pk_fp8_f32 v21, v28, v29 op_sel:[0,0,1]
	v_lshlrev_b64 v[24:25], 10, v[24:25]
	v_med3_f32 v99, v99, s55, v213
	v_med3_f32 v98, v98, s55, v213
	v_cvt_pk_fp8_f32 v102, v30, v31
	v_lshl_add_u64 v[24:25], s[2:3], 0, v[24:25]
	v_pk_add_f32 v[98:99], v[98:99], 1.0 op_sel_hi:[1,0]
	v_lshl_add_u64 v[24:25], v[24:25], 0, v[18:19]
	v_pk_mul_f32 v[26:27], v[96:97], v[98:99]
	v_or_b32_e32 v20, 48, v20
	v_pk_mul_f32 v[26:27], v[26:27], v[100:101]
	s_waitcnt lgkmcnt(0)
	global_store_dwordx2 v[24:25], v[22:23], off
	ds_bpermute_b32 v22, v167, v21
	v_ashrrev_i32_e32 v21, 31, v20
	v_cvt_pk_fp8_f32 v102, v26, v27 op_sel:[0,0,1]
	v_lshlrev_b64 v[20:21], 10, v[20:21]
	v_lshl_add_u64 v[20:21], s[2:3], 0, v[20:21]
	v_lshl_add_u64 v[18:19], v[20:21], 0, v[18:19]
	v_pk_fma_f32 v[20:21], v[92:93], s[38:39], v[12:13] op_sel_hi:[1,0,1]
	ds_bpermute_b32 v23, v167, v102
	v_min_f32_e32 v21, 0x40e00000, v21
	v_min_f32_e32 v20, 0x40e00000, v20
	v_pk_mul_f32 v[24:25], v[20:21], s[88:89] op_sel_hi:[1,0]
	v_exp_f32_e32 v24, v24
	v_exp_f32_e32 v25, v25
	s_waitcnt lgkmcnt(0)
	global_store_dwordx2 v[18:19], v[22:23], off
	v_pk_fma_f32 v[18:19], v[88:89], s[38:39], v[8:9] op_sel_hi:[1,0,1]
	v_pk_fma_f32 v[28:29], v[82:83], s[38:39], v[6:7] op_sel_hi:[1,0,1]
	v_pk_add_f32 v[22:23], v[24:25], 1.0 op_sel_hi:[1,0]
	v_med3_f32 v19, v19, s55, v213
	v_rcp_f32_e32 v22, v22
	v_rcp_f32_e32 v23, v23
	v_med3_f32 v18, v18, s55, v213
	v_pk_add_f32 v[18:19], v[18:19], 1.0 op_sel_hi:[1,0]
	v_pk_fma_f32 v[24:25], v[90:91], s[38:39], v[10:11] op_sel_hi:[1,0,1]
	v_pk_mul_f32 v[18:19], v[20:21], v[18:19]
	v_pk_fma_f32 v[20:21], v[94:95], s[38:39], v[14:15] op_sel_hi:[1,0,1]
	v_pk_mul_f32 v[18:19], v[18:19], v[22:23]
	v_min_f32_e32 v21, 0x40e00000, v21
	v_min_f32_e32 v20, 0x40e00000, v20
	v_pk_mul_f32 v[22:23], v[20:21], s[88:89] op_sel_hi:[1,0]
	v_med3_f32 v25, v25, s55, v213
	v_med3_f32 v24, v24, s55, v213
	v_exp_f32_e32 v22, v22
	v_exp_f32_e32 v23, v23
	v_pk_add_f32 v[24:25], v[24:25], 1.0 op_sel_hi:[1,0]
	v_cvt_pk_fp8_f32 v30, v18, v19
	v_pk_mul_f32 v[20:21], v[20:21], v[24:25]
	v_pk_fma_f32 v[24:25], v[84:85], s[38:39], v[0:1] op_sel_hi:[1,0,1]
	v_pk_add_f32 v[22:23], v[22:23], 1.0 op_sel_hi:[1,0]
	v_min_f32_e32 v25, 0x40e00000, v25
	v_min_f32_e32 v24, 0x40e00000, v24
	v_pk_mul_f32 v[26:27], v[24:25], s[88:89] op_sel_hi:[1,0]
	v_rcp_f32_e32 v22, v22
	v_exp_f32_e32 v26, v26
	v_exp_f32_e32 v27, v27
	v_rcp_f32_e32 v23, v23
	v_med3_f32 v29, v29, s55, v213
	v_med3_f32 v28, v28, s55, v213
	v_pk_add_f32 v[26:27], v[26:27], 1.0 op_sel_hi:[1,0]
	v_pk_mul_f32 v[20:21], v[20:21], v[22:23]
	v_pk_fma_f32 v[22:23], v[80:81], s[38:39], v[4:5] op_sel_hi:[1,0,1]
	v_rcp_f32_e32 v26, v26
	v_rcp_f32_e32 v27, v27
	v_med3_f32 v23, v23, s55, v213
	v_med3_f32 v22, v22, s55, v213
	v_pk_add_f32 v[22:23], v[22:23], 1.0 op_sel_hi:[1,0]
	v_cvt_pk_fp8_f32 v30, v20, v21 op_sel:[0,0,1]
	v_pk_mul_f32 v[22:23], v[24:25], v[22:23]
	v_pk_fma_f32 v[20:21], v[76:77], s[38:39], v[12:13] op_sel_hi:[1,0,1]
	v_pk_mul_f32 v[22:23], v[22:23], v[26:27]
	v_pk_add_f32 v[18:19], v[28:29], 1.0 op_sel_hi:[1,0]
	v_min_f32_e32 v21, 0x40e00000, v21
	v_min_f32_e32 v20, 0x40e00000, v20
	v_pk_fma_f32 v[24:25], v[86:87], s[38:39], v[2:3] op_sel_hi:[1,0,1]
	v_cvt_pk_fp8_f32 v28, v22, v23
	v_pk_mul_f32 v[22:23], v[20:21], s[88:89] op_sel_hi:[1,0]
	v_min_f32_e32 v25, 0x40e00000, v25
	v_min_f32_e32 v24, 0x40e00000, v24
	v_exp_f32_e32 v22, v22
	v_exp_f32_e32 v23, v23
	v_pk_mul_f32 v[26:27], v[24:25], s[88:89] op_sel_hi:[1,0]
	v_pk_mul_f32 v[18:19], v[24:25], v[18:19]
	v_exp_f32_e32 v26, v26
	v_exp_f32_e32 v27, v27
	v_pk_add_f32 v[22:23], v[22:23], 1.0 op_sel_hi:[1,0]
	v_pk_fma_f32 v[24:25], v[72:73], s[38:39], v[8:9] op_sel_hi:[1,0,1]
	v_rcp_f32_e32 v22, v22
	v_rcp_f32_e32 v23, v23
	v_pk_add_f32 v[26:27], v[26:27], 1.0 op_sel_hi:[1,0]
	v_med3_f32 v25, v25, s55, v213
	v_med3_f32 v24, v24, s55, v213
	v_rcp_f32_e32 v26, v26
	v_rcp_f32_e32 v27, v27
	v_pk_add_f32 v[24:25], v[24:25], 1.0 op_sel_hi:[1,0]
	s_mov_b32 s0, 0x20000
	v_pk_mul_f32 v[20:21], v[20:21], v[24:25]
	v_pk_mul_f32 v[18:19], v[18:19], v[26:27]
	v_pk_mul_f32 v[20:21], v[20:21], v[22:23]
	v_pk_fma_f32 v[22:23], v[78:79], s[38:39], v[14:15] op_sel_hi:[1,0,1]
	v_pk_fma_f32 v[26:27], v[74:75], s[38:39], v[10:11] op_sel_hi:[1,0,1]
	v_min_f32_e32 v23, 0x40e00000, v23
	v_min_f32_e32 v22, 0x40e00000, v22
	v_pk_mul_f32 v[24:25], v[22:23], s[88:89] op_sel_hi:[1,0]
	v_cvt_pk_fp8_f32 v28, v18, v19 op_sel:[0,0,1]
	v_exp_f32_e32 v24, v24
	v_exp_f32_e32 v25, v25
	v_med3_f32 v27, v27, s55, v213
	v_med3_f32 v26, v26, s55, v213
	v_pk_add_f32 v[26:27], v[26:27], 1.0 op_sel_hi:[1,0]
	ds_bpermute_b32 v19, v167, v28
	v_pk_mul_f32 v[22:23], v[22:23], v[26:27]
	v_pk_fma_f32 v[26:27], v[68:69], s[38:39], v[0:1] op_sel_hi:[1,0,1]
	v_pk_add_f32 v[24:25], v[24:25], 1.0 op_sel_hi:[1,0]
	v_min_f32_e32 v27, 0x40e00000, v27
	v_min_f32_e32 v26, 0x40e00000, v26
	v_pk_mul_f32 v[28:29], v[26:27], s[88:89] op_sel_hi:[1,0]
	v_rcp_f32_e32 v24, v24
	v_rcp_f32_e32 v25, v25
	v_exp_f32_e32 v28, v28
	v_exp_f32_e32 v29, v29
	ds_bpermute_b32 v18, v167, v30
	v_pk_mul_f32 v[22:23], v[22:23], v[24:25]
	v_pk_fma_f32 v[24:25], v[64:65], s[38:39], v[4:5] op_sel_hi:[1,0,1]
	v_pk_add_f32 v[28:29], v[28:29], 1.0 op_sel_hi:[1,0]
	v_med3_f32 v25, v25, s55, v213
	v_rcp_f32_e32 v28, v28
	v_rcp_f32_e32 v29, v29
	v_med3_f32 v24, v24, s55, v213
	v_pk_add_f32 v[24:25], v[24:25], 1.0 op_sel_hi:[1,0]
	v_pk_fma_f32 v[30:31], v[66:67], s[38:39], v[6:7] op_sel_hi:[1,0,1]
	v_pk_mul_f32 v[24:25], v[26:27], v[24:25]
	v_pk_fma_f32 v[26:27], v[70:71], s[38:39], v[2:3] op_sel_hi:[1,0,1]
	v_pk_mul_f32 v[24:25], v[24:25], v[28:29]
	v_min_f32_e32 v27, 0x40e00000, v27
	v_min_f32_e32 v26, 0x40e00000, v26
	v_pk_mul_f32 v[28:29], v[26:27], s[88:89] op_sel_hi:[1,0]
	v_exp_f32_e32 v28, v28
	v_exp_f32_e32 v29, v29
	v_med3_f32 v31, v31, s55, v213
	v_med3_f32 v30, v30, s55, v213
	v_pk_add_f32 v[28:29], v[28:29], 1.0 op_sel_hi:[1,0]
	v_cvt_pk_fp8_f32 v64, v20, v21
	v_rcp_f32_e32 v28, v28
	v_rcp_f32_e32 v29, v29
	v_cvt_pk_fp8_f32 v65, v24, v25
	v_pk_add_f32 v[30:31], v[30:31], 1.0 op_sel_hi:[1,0]
	v_cvt_pk_fp8_f32 v64, v22, v23 op_sel:[0,0,1]
	v_pk_mul_f32 v[20:21], v[26:27], v[30:31]
	v_pk_fma_f32 v[22:23], v[60:61], s[38:39], v[12:13] op_sel_hi:[1,0,1]
	v_pk_mul_f32 v[20:21], v[20:21], v[28:29]
	v_min_f32_e32 v23, 0x40e00000, v23
	v_cvt_pk_fp8_f32 v65, v20, v21 op_sel:[0,0,1]
	v_add_co_u32_e32 v20, vcc, s0, v16
	v_min_f32_e32 v22, 0x40e00000, v22
	s_nop 0
	v_addc_co_u32_e32 v21, vcc, 0, v17, vcc
	s_waitcnt lgkmcnt(0)
	global_store_dwordx2 v[20:21], v[18:19], off
	ds_bpermute_b32 v18, v167, v64
	ds_bpermute_b32 v19, v167, v65
	v_pk_mul_f32 v[24:25], v[22:23], s[88:89] op_sel_hi:[1,0]
	s_mov_b32 s2, 0x24000
	v_exp_f32_e32 v24, v24
	v_exp_f32_e32 v25, v25
	v_add_co_u32_e32 v20, vcc, s2, v16
	s_nop 0
	v_addc_co_u32_e32 v21, vcc, 0, v17, vcc
	s_waitcnt lgkmcnt(0)
	global_store_dwordx2 v[20:21], v[18:19], off
	v_pk_add_f32 v[20:21], v[24:25], 1.0 op_sel_hi:[1,0]
	v_pk_fma_f32 v[18:19], v[56:57], s[38:39], v[8:9] op_sel_hi:[1,0,1]
	v_rcp_f32_e32 v20, v20
	v_rcp_f32_e32 v21, v21
	v_med3_f32 v19, v19, s55, v213
	v_med3_f32 v18, v18, s55, v213
	v_pk_add_f32 v[18:19], v[18:19], 1.0 op_sel_hi:[1,0]
	v_pk_fma_f32 v[24:25], v[58:59], s[38:39], v[10:11] op_sel_hi:[1,0,1]
	v_pk_mul_f32 v[18:19], v[22:23], v[18:19]
	v_med3_f32 v25, v25, s55, v213
	v_pk_mul_f32 v[18:19], v[18:19], v[20:21]
	v_pk_fma_f32 v[20:21], v[62:63], s[38:39], v[14:15] op_sel_hi:[1,0,1]
	v_med3_f32 v24, v24, s55, v213
	v_min_f32_e32 v21, 0x40e00000, v21
	v_min_f32_e32 v20, 0x40e00000, v20
	v_pk_mul_f32 v[22:23], v[20:21], s[88:89] op_sel_hi:[1,0]
	v_pk_add_f32 v[24:25], v[24:25], 1.0 op_sel_hi:[1,0]
	v_exp_f32_e32 v22, v22
	v_exp_f32_e32 v23, v23
	v_pk_mul_f32 v[20:21], v[20:21], v[24:25]
	v_pk_fma_f32 v[24:25], v[52:53], s[38:39], v[0:1] op_sel_hi:[1,0,1]
	v_cvt_pk_fp8_f32 v30, v18, v19
	v_min_f32_e32 v25, 0x40e00000, v25
	v_min_f32_e32 v24, 0x40e00000, v24
	v_pk_add_f32 v[22:23], v[22:23], 1.0 op_sel_hi:[1,0]
	v_pk_mul_f32 v[26:27], v[24:25], s[88:89] op_sel_hi:[1,0]
	v_rcp_f32_e32 v22, v22
	v_rcp_f32_e32 v23, v23
	v_exp_f32_e32 v26, v26
	v_exp_f32_e32 v27, v27
	v_pk_fma_f32 v[8:9], v[40:41], s[38:39], v[8:9] op_sel_hi:[1,0,1]
	v_pk_mul_f32 v[20:21], v[20:21], v[22:23]
	v_pk_fma_f32 v[22:23], v[48:49], s[38:39], v[4:5] op_sel_hi:[1,0,1]
	v_pk_add_f32 v[26:27], v[26:27], 1.0 op_sel_hi:[1,0]
	v_med3_f32 v23, v23, s55, v213
	v_rcp_f32_e32 v26, v26
	v_rcp_f32_e32 v27, v27
	v_med3_f32 v22, v22, s55, v213
	v_pk_fma_f32 v[12:13], v[44:45], s[38:39], v[12:13] op_sel_hi:[1,0,1]
	v_med3_f32 v9, v9, s55, v213
	v_med3_f32 v8, v8, s55, v213
	v_pk_add_f32 v[22:23], v[22:23], 1.0 op_sel_hi:[1,0]
	v_min_f32_e32 v13, 0x40e00000, v13
	v_min_f32_e32 v12, 0x40e00000, v12
	v_pk_add_f32 v[8:9], v[8:9], 1.0 op_sel_hi:[1,0]
	v_pk_fma_f32 v[10:11], v[42:43], s[38:39], v[10:11] op_sel_hi:[1,0,1]
	v_pk_mul_f32 v[22:23], v[24:25], v[22:23]
	v_pk_fma_f32 v[24:25], v[54:55], s[38:39], v[2:3] op_sel_hi:[1,0,1]
	v_cvt_pk_fp8_f32 v30, v20, v21 op_sel:[0,0,1]
	v_pk_mul_f32 v[20:21], v[12:13], s[88:89] op_sel_hi:[1,0]
	v_pk_mul_f32 v[8:9], v[12:13], v[8:9]
	v_pk_fma_f32 v[12:13], v[46:47], s[38:39], v[14:15] op_sel_hi:[1,0,1]
	v_med3_f32 v11, v11, s55, v213
	v_med3_f32 v10, v10, s55, v213
	v_pk_fma_f32 v[0:1], v[36:37], s[38:39], v[0:1] op_sel_hi:[1,0,1]
	v_min_f32_e32 v25, 0x40e00000, v25
	v_min_f32_e32 v24, 0x40e00000, v24
	v_min_f32_e32 v13, 0x40e00000, v13
	v_min_f32_e32 v12, 0x40e00000, v12
	v_pk_add_f32 v[10:11], v[10:11], 1.0 op_sel_hi:[1,0]
	v_min_f32_e32 v1, 0x40e00000, v1
	v_min_f32_e32 v0, 0x40e00000, v0
	v_pk_mul_f32 v[22:23], v[22:23], v[26:27]
	v_pk_mul_f32 v[26:27], v[24:25], s[88:89] op_sel_hi:[1,0]
	v_pk_mul_f32 v[14:15], v[12:13], s[88:89] op_sel_hi:[1,0]
	v_pk_mul_f32 v[10:11], v[12:13], v[10:11]
	v_pk_mul_f32 v[12:13], v[0:1], s[88:89] op_sel_hi:[1,0]
	v_exp_f32_e32 v26, v26
	v_exp_f32_e32 v27, v27
	v_exp_f32_e32 v20, v20
	v_exp_f32_e32 v21, v21
	v_exp_f32_e32 v12, v12
	v_exp_f32_e32 v13, v13
	v_pk_fma_f32 v[4:5], v[32:33], s[38:39], v[4:5] op_sel_hi:[1,0,1]
	v_pk_fma_f32 v[2:3], v[38:39], s[38:39], v[2:3] op_sel_hi:[1,0,1]
	v_med3_f32 v5, v5, s55, v213
	v_med3_f32 v4, v4, s55, v213
	v_pk_fma_f32 v[28:29], v[50:51], s[38:39], v[6:7] op_sel_hi:[1,0,1]
	v_pk_add_f32 v[4:5], v[4:5], 1.0 op_sel_hi:[1,0]
	v_min_f32_e32 v3, 0x40e00000, v3
	v_min_f32_e32 v2, 0x40e00000, v2
	v_med3_f32 v29, v29, s55, v213
	v_med3_f32 v28, v28, s55, v213
	v_pk_add_f32 v[26:27], v[26:27], 1.0 op_sel_hi:[1,0]
	v_pk_add_f32 v[20:21], v[20:21], 1.0 op_sel_hi:[1,0]
	v_pk_add_f32 v[12:13], v[12:13], 1.0 op_sel_hi:[1,0]
	v_pk_mul_f32 v[0:1], v[0:1], v[4:5]
	v_pk_mul_f32 v[4:5], v[2:3], s[88:89] op_sel_hi:[1,0]
	v_rcp_f32_e32 v26, v26
	v_rcp_f32_e32 v27, v27
	v_pk_add_f32 v[18:19], v[28:29], 1.0 op_sel_hi:[1,0]
	v_rcp_f32_e32 v20, v20
	v_rcp_f32_e32 v21, v21
	v_exp_f32_e32 v14, v14
	v_exp_f32_e32 v15, v15
	v_rcp_f32_e32 v12, v12
	v_rcp_f32_e32 v13, v13
	v_exp_f32_e32 v4, v4
	v_exp_f32_e32 v5, v5
	v_cvt_pk_fp8_f32 v28, v22, v23
	v_pk_mul_f32 v[18:19], v[24:25], v[18:19]
	v_pk_mul_f32 v[8:9], v[8:9], v[20:21]
	v_pk_mul_f32 v[18:19], v[18:19], v[26:27]
	v_pk_add_f32 v[14:15], v[14:15], 1.0 op_sel_hi:[1,0]
	v_pk_mul_f32 v[0:1], v[0:1], v[12:13]
	v_pk_add_f32 v[4:5], v[4:5], 1.0 op_sel_hi:[1,0]
	v_cvt_pk_fp8_f32 v28, v18, v19 op_sel:[0,0,1]
	v_rcp_f32_e32 v14, v14
	v_rcp_f32_e32 v15, v15
	v_pk_fma_f32 v[6:7], v[34:35], s[38:39], v[6:7] op_sel_hi:[1,0,1]
	v_rcp_f32_e32 v4, v4
	v_rcp_f32_e32 v5, v5
	v_cvt_pk_fp8_f32 v12, v8, v9
	v_med3_f32 v7, v7, s55, v213
	v_med3_f32 v6, v6, s55, v213
	v_cvt_pk_fp8_f32 v8, v0, v1
	v_pk_add_f32 v[6:7], v[6:7], 1.0 op_sel_hi:[1,0]
	ds_bpermute_b32 v18, v167, v30
	v_pk_mul_f32 v[0:1], v[2:3], v[6:7]
	ds_bpermute_b32 v19, v167, v28
	v_pk_mul_f32 v[10:11], v[10:11], v[14:15]
	v_pk_mul_f32 v[0:1], v[0:1], v[4:5]
	v_cvt_pk_fp8_f32 v12, v10, v11 op_sel:[0,0,1]
	v_cvt_pk_fp8_f32 v8, v0, v1 op_sel:[0,0,1]
	s_mov_b32 s2, 0x28000
	v_add_co_u32_e32 v0, vcc, s2, v16
	v_mov_b32_e32 v174, v218
	s_nop 0
	v_addc_co_u32_e32 v1, vcc, 0, v17, vcc
	s_waitcnt lgkmcnt(0)
	global_store_dwordx2 v[0:1], v[18:19], off
	ds_bpermute_b32 v0, v167, v12
	ds_bpermute_b32 v1, v167, v8
	v_add_co_u32_e32 v2, vcc, 0x2c000, v16
	v_mov_b32_e32 v168, v216
	s_nop 0
	v_addc_co_u32_e32 v3, vcc, 0, v17, vcc
	s_and_b64 vcc, exec, s[14:15]
	v_mov_b32_e32 v170, v217
	v_mov_b32_e32 v166, v215
	v_mov_b32_e32 v219, v197
	v_mov_b32_e32 v220, v196
	s_mov_b64 s[24:25], s[16:17]
	s_mov_b64 s[22:23], s[18:19]
	s_mov_b32 s57, s1
	v_readlane_b32 s64, v255, 32
	s_movk_i32 s72, 0x48
	s_waitcnt lgkmcnt(0)
	global_store_dwordx2 v[2:3], v[0:1], off
	s_cbranch_vccnz .LBB0_1563

.LBB0_1655:
	s_mul_hi_u32 s7, s82, 0xaaaaaaab
	s_lshr_b32 s7, s7, 1
	s_mul_i32 s7, s7, 3
	s_sub_i32 s7, s82, s7
	v_lshl_add_u32 v30, s7, 10, v175
	ds_read_b128 v[4:7], v30
	ds_read_b128 v[8:11], v30 offset:16
	s_mov_b32 s0, 0x41000000
	v_lshl_or_b32 v2, s14, 8, v194
	s_waitcnt lgkmcnt(0)
	v_pk_mul_f32 v[20:21], v[4:5], s[0:1] op_sel_hi:[1,0]
	v_pk_mul_f32 v[22:23], v[8:9], s[0:1] op_sel_hi:[1,0]
	v_pk_mul_f32 v[18:19], v[6:7], s[0:1] op_sel_hi:[1,0]
	v_pk_fma_f32 v[0:1], v[156:157], s[74:75], v[20:21] op_sel_hi:[1,0,1]
	v_pk_fma_f32 v[4:5], v[152:153], s[74:75], v[22:23] op_sel_hi:[1,0,1]
	v_cvt_pk_fp8_f32 v6, v0, v1
	v_cvt_pk_fp8_f32 v7, v4, v5
	v_pk_mul_f32 v[24:25], v[10:11], s[0:1] op_sel_hi:[1,0]
	v_pk_fma_f32 v[0:1], v[158:159], s[74:75], v[18:19] op_sel_hi:[1,0,1]
	v_pk_fma_f32 v[4:5], v[154:155], s[74:75], v[24:25] op_sel_hi:[1,0,1]
	v_cvt_pk_fp8_f32 v6, v0, v1 op_sel:[0,0,1]
	v_cvt_pk_fp8_f32 v7, v4, v5 op_sel:[0,0,1]
	v_lshl_add_u32 v8, s12, 8, v193
	v_ashrrev_i32_e32 v9, 31, v8
	ds_bpermute_b32 v0, v169, v6
	ds_bpermute_b32 v1, v169, v7
	v_lshlrev_b64 v[4:5], 10, v[8:9]
	v_pk_fma_f32 v[6:7], v[148:149], s[74:75], v[20:21] op_sel_hi:[1,0,1]
	v_cvt_pk_fp8_f32 v9, v6, v7
	v_pk_fma_f32 v[10:11], v[144:145], s[74:75], v[22:23] op_sel_hi:[1,0,1]
	v_pk_fma_f32 v[6:7], v[150:151], s[74:75], v[18:19] op_sel_hi:[1,0,1]
	v_cvt_pk_fp8_f32 v12, v10, v11
	v_cvt_pk_fp8_f32 v9, v6, v7 op_sel:[0,0,1]
	v_ashrrev_i32_e32 v3, 31, v2
	v_lshl_add_u64 v[4:5], s[68:69], 0, v[4:5]
	v_pk_fma_f32 v[10:11], v[146:147], s[74:75], v[24:25] op_sel_hi:[1,0,1]
	v_lshl_add_u64 v[14:15], v[4:5], 0, v[2:3]
	v_cvt_pk_fp8_f32 v12, v10, v11 op_sel:[0,0,1]
	s_waitcnt lgkmcnt(0)
	global_store_dwordx2 v[14:15], v[0:1], off
	ds_bpermute_b32 v0, v169, v9
	v_pk_fma_f32 v[6:7], v[140:141], s[74:75], v[20:21] op_sel_hi:[1,0,1]
	v_cvt_pk_fp8_f32 v9, v6, v7
	ds_bpermute_b32 v1, v169, v12
	v_or_b32_e32 v4, 16, v8
	v_pk_fma_f32 v[10:11], v[136:137], s[74:75], v[22:23] op_sel_hi:[1,0,1]
	v_pk_fma_f32 v[6:7], v[142:143], s[74:75], v[18:19] op_sel_hi:[1,0,1]
	v_ashrrev_i32_e32 v5, 31, v4
	v_cvt_pk_fp8_f32 v12, v10, v11
	v_cvt_pk_fp8_f32 v9, v6, v7 op_sel:[0,0,1]
	v_lshlrev_b64 v[4:5], 10, v[4:5]
	v_lshl_add_u64 v[4:5], s[68:69], 0, v[4:5]
	v_pk_fma_f32 v[10:11], v[138:139], s[74:75], v[24:25] op_sel_hi:[1,0,1]
	v_lshl_add_u64 v[6:7], v[4:5], 0, v[2:3]
	v_cvt_pk_fp8_f32 v12, v10, v11 op_sel:[0,0,1]
	s_waitcnt lgkmcnt(0)
	global_store_dwordx2 v[6:7], v[0:1], off
	ds_bpermute_b32 v0, v169, v9
	v_pk_fma_f32 v[10:11], v[132:133], s[74:75], v[20:21] op_sel_hi:[1,0,1]
	v_cvt_pk_fp8_f32 v9, v10, v11
	ds_bpermute_b32 v1, v169, v12
	v_pk_fma_f32 v[12:13], v[128:129], s[74:75], v[22:23] op_sel_hi:[1,0,1]
	v_pk_fma_f32 v[10:11], v[134:135], s[74:75], v[18:19] op_sel_hi:[1,0,1]
	v_or_b32_e32 v4, 32, v8
	v_cvt_pk_fp8_f32 v16, v12, v13
	v_cvt_pk_fp8_f32 v9, v10, v11 op_sel:[0,0,1]
	v_ashrrev_i32_e32 v5, 31, v4
	v_lshlrev_b64 v[4:5], 10, v[4:5]
	v_lshl_add_u64 v[4:5], s[68:69], 0, v[4:5]
	v_pk_fma_f32 v[12:13], v[130:131], s[74:75], v[24:25] op_sel_hi:[1,0,1]
	v_pk_fma_f32 v[10:11], v[124:125], s[74:75], v[20:21] op_sel_hi:[1,0,1]
	v_cvt_pk_fp8_f32 v16, v12, v13 op_sel:[0,0,1]
	v_lshl_add_u64 v[12:13], v[4:5], 0, v[2:3]
	ds_bpermute_b32 v4, v169, v9
	v_cvt_pk_fp8_f32 v9, v10, v11
	ds_bpermute_b32 v5, v169, v16
	v_pk_fma_f32 v[16:17], v[120:121], s[74:75], v[22:23] op_sel_hi:[1,0,1]
	v_pk_fma_f32 v[10:11], v[126:127], s[74:75], v[18:19] op_sel_hi:[1,0,1]
	v_cvt_pk_fp8_f32 v26, v16, v17
	v_cvt_pk_fp8_f32 v9, v10, v11 op_sel:[0,0,1]
	v_pk_fma_f32 v[16:17], v[122:123], s[74:75], v[24:25] op_sel_hi:[1,0,1]
	v_cvt_pk_fp8_f32 v26, v16, v17 op_sel:[0,0,1]
	ds_bpermute_b32 v10, v169, v9
	v_pk_fma_f32 v[16:17], v[116:117], s[74:75], v[20:21] op_sel_hi:[1,0,1]
	v_cvt_pk_fp8_f32 v9, v16, v17
	ds_bpermute_b32 v11, v169, v26
	v_pk_fma_f32 v[26:27], v[112:113], s[74:75], v[22:23] op_sel_hi:[1,0,1]
	v_pk_fma_f32 v[16:17], v[118:119], s[74:75], v[18:19] op_sel_hi:[1,0,1]
	v_cvt_pk_fp8_f32 v28, v26, v27
	v_cvt_pk_fp8_f32 v9, v16, v17 op_sel:[0,0,1]
	v_pk_fma_f32 v[26:27], v[114:115], s[74:75], v[24:25] op_sel_hi:[1,0,1]
	s_waitcnt lgkmcnt(0)
	global_store_dwordx2 v[12:13], v[0:1], off
	v_or_b32_e32 v0, 48, v8
	v_cvt_pk_fp8_f32 v28, v26, v27 op_sel:[0,0,1]
	ds_bpermute_b32 v16, v169, v9
	v_pk_fma_f32 v[26:27], v[108:109], s[74:75], v[20:21] op_sel_hi:[1,0,1]
	v_ashrrev_i32_e32 v1, 31, v0
	v_cvt_pk_fp8_f32 v9, v26, v27
	v_lshlrev_b64 v[0:1], 10, v[0:1]
	v_lshl_add_u64 v[0:1], s[68:69], 0, v[0:1]
	v_lshl_add_u64 v[0:1], v[0:1], 0, v[2:3]
	ds_bpermute_b32 v17, v169, v28
	v_pk_fma_f32 v[28:29], v[104:105], s[74:75], v[22:23] op_sel_hi:[1,0,1]
	v_pk_fma_f32 v[26:27], v[110:111], s[74:75], v[18:19] op_sel_hi:[1,0,1]
	global_store_dwordx2 v[0:1], v[4:5], off
	v_add_u32_e32 v4, 0x80, v8
	v_cvt_pk_fp8_f32 v31, v28, v29
	v_cvt_pk_fp8_f32 v9, v26, v27 op_sel:[0,0,1]
	v_ashrrev_i32_e32 v5, 31, v4
	v_lshlrev_b64 v[4:5], 10, v[4:5]
	v_lshl_add_u64 v[4:5], s[68:69], 0, v[4:5]
	v_pk_fma_f32 v[28:29], v[106:107], s[74:75], v[24:25] op_sel_hi:[1,0,1]
	v_lshl_add_u64 v[4:5], v[4:5], 0, v[2:3]
	v_cvt_pk_fp8_f32 v31, v28, v29 op_sel:[0,0,1]
	ds_bpermute_b32 v26, v169, v9
	v_pk_fma_f32 v[20:21], v[92:93], s[74:75], v[20:21] op_sel_hi:[1,0,1]
	v_pk_fma_f32 v[22:23], v[88:89], s[74:75], v[22:23] op_sel_hi:[1,0,1]
	global_store_dwordx2 v[4:5], v[10:11], off
	v_add_u32_e32 v10, 0x90, v8
	v_cvt_pk_fp8_f32 v9, v20, v21
	v_cvt_pk_fp8_f32 v28, v22, v23
	v_ashrrev_i32_e32 v11, 31, v10
	v_lshlrev_b64 v[10:11], 10, v[10:11]
	v_lshl_add_u64 v[10:11], s[68:69], 0, v[10:11]
	v_pk_fma_f32 v[18:19], v[94:95], s[74:75], v[18:19] op_sel_hi:[1,0,1]
	v_pk_fma_f32 v[20:21], v[90:91], s[74:75], v[24:25] op_sel_hi:[1,0,1]
	v_lshl_add_u64 v[10:11], v[10:11], 0, v[2:3]
	v_cvt_pk_fp8_f32 v9, v18, v19 op_sel:[0,0,1]
	v_cvt_pk_fp8_f32 v28, v20, v21 op_sel:[0,0,1]
	ds_read_b128 v[18:21], v30 offset:512
	ds_read_b128 v[22:25], v30 offset:528
	s_waitcnt lgkmcnt(0)
	global_store_dwordx2 v[10:11], v[16:17], off
	ds_bpermute_b32 v27, v169, v31
	v_add_u32_e32 v16, 0xa0, v8
	v_ashrrev_i32_e32 v17, 31, v16
	v_lshlrev_b64 v[16:17], 10, v[16:17]
	v_lshl_add_u64 v[16:17], s[68:69], 0, v[16:17]
	v_lshl_add_u64 v[16:17], v[16:17], 0, v[2:3]
	v_pk_mul_f32 v[18:19], v[18:19], s[0:1] op_sel_hi:[1,0]
	v_pk_mul_f32 v[22:23], v[22:23], s[0:1] op_sel_hi:[1,0]
	s_waitcnt lgkmcnt(0)
	global_store_dwordx2 v[16:17], v[26:27], off
	ds_bpermute_b32 v27, v169, v28
	v_pk_fma_f32 v[28:29], v[100:101], s[74:75], v[18:19] op_sel_hi:[1,0,1]
	v_pk_fma_f32 v[30:31], v[96:97], s[74:75], v[22:23] op_sel_hi:[1,0,1]
	v_cvt_pk_fp8_f32 v88, v28, v29
	v_cvt_pk_fp8_f32 v89, v30, v31
	v_pk_mul_f32 v[20:21], v[20:21], s[0:1] op_sel_hi:[1,0]
	v_pk_mul_f32 v[24:25], v[24:25], s[0:1] op_sel_hi:[1,0]
	v_pk_fma_f32 v[28:29], v[102:103], s[74:75], v[20:21] op_sel_hi:[1,0,1]
	v_pk_fma_f32 v[30:31], v[98:99], s[74:75], v[24:25] op_sel_hi:[1,0,1]
	v_cvt_pk_fp8_f32 v88, v28, v29 op_sel:[0,0,1]
	v_cvt_pk_fp8_f32 v89, v30, v31 op_sel:[0,0,1]
	ds_bpermute_b32 v26, v169, v9
	v_add_u32_e32 v8, 0xb0, v8
	v_ashrrev_i32_e32 v9, 31, v8
	ds_bpermute_b32 v28, v169, v88
	ds_bpermute_b32 v29, v169, v89
	v_lshlrev_b64 v[8:9], 10, v[8:9]
	v_lshl_add_u64 v[8:9], s[68:69], 0, v[8:9]
	v_lshl_add_u64 v[2:3], v[8:9], 0, v[2:3]
	s_waitcnt lgkmcnt(0)
	global_store_dwordx2 v[2:3], v[26:27], off
	global_store_dwordx2 v[14:15], v[28:29], off offset:128
	v_pk_fma_f32 v[8:9], v[84:85], s[74:75], v[18:19] op_sel_hi:[1,0,1]
	v_pk_fma_f32 v[14:15], v[80:81], s[74:75], v[22:23] op_sel_hi:[1,0,1]
	v_cvt_pk_fp8_f32 v26, v8, v9
	v_cvt_pk_fp8_f32 v27, v14, v15
	v_pk_fma_f32 v[8:9], v[86:87], s[74:75], v[20:21] op_sel_hi:[1,0,1]
	v_pk_fma_f32 v[14:15], v[82:83], s[74:75], v[24:25] op_sel_hi:[1,0,1]
	v_cvt_pk_fp8_f32 v26, v8, v9 op_sel:[0,0,1]
	v_cvt_pk_fp8_f32 v27, v14, v15 op_sel:[0,0,1]
	v_pk_fma_f32 v[8:9], v[76:77], s[74:75], v[18:19] op_sel_hi:[1,0,1]
	v_pk_fma_f32 v[14:15], v[72:73], s[74:75], v[22:23] op_sel_hi:[1,0,1]
	v_cvt_pk_fp8_f32 v28, v8, v9
	v_cvt_pk_fp8_f32 v29, v14, v15
	v_pk_fma_f32 v[8:9], v[78:79], s[74:75], v[20:21] op_sel_hi:[1,0,1]
	v_pk_fma_f32 v[14:15], v[74:75], s[74:75], v[24:25] op_sel_hi:[1,0,1]
	v_cvt_pk_fp8_f32 v28, v8, v9 op_sel:[0,0,1]
	v_cvt_pk_fp8_f32 v29, v14, v15 op_sel:[0,0,1]
	ds_bpermute_b32 v8, v169, v26
	ds_bpermute_b32 v9, v169, v27
	ds_bpermute_b32 v14, v169, v28
	ds_bpermute_b32 v15, v169, v29
	v_pk_fma_f32 v[26:27], v[68:69], s[74:75], v[18:19] op_sel_hi:[1,0,1]
	s_waitcnt lgkmcnt(0)
	global_store_dwordx2 v[6:7], v[8:9], off offset:128
	global_store_dwordx2 v[12:13], v[14:15], off offset:128
	v_pk_fma_f32 v[8:9], v[60:61], s[74:75], v[18:19] op_sel_hi:[1,0,1]
	v_pk_fma_f32 v[12:13], v[56:57], s[74:75], v[22:23] op_sel_hi:[1,0,1]
	v_cvt_pk_fp8_f32 v30, v26, v27
	v_cvt_pk_fp8_f32 v14, v8, v9
	v_cvt_pk_fp8_f32 v15, v12, v13
	v_pk_fma_f32 v[26:27], v[70:71], s[74:75], v[20:21] op_sel_hi:[1,0,1]
	v_pk_fma_f32 v[8:9], v[62:63], s[74:75], v[20:21] op_sel_hi:[1,0,1]
	v_pk_fma_f32 v[12:13], v[58:59], s[74:75], v[24:25] op_sel_hi:[1,0,1]
	v_pk_fma_f32 v[28:29], v[64:65], s[74:75], v[22:23] op_sel_hi:[1,0,1]
	v_cvt_pk_fp8_f32 v30, v26, v27 op_sel:[0,0,1]
	v_cvt_pk_fp8_f32 v14, v8, v9 op_sel:[0,0,1]
	v_cvt_pk_fp8_f32 v15, v12, v13 op_sel:[0,0,1]
	v_pk_fma_f32 v[8:9], v[52:53], s[74:75], v[18:19] op_sel_hi:[1,0,1]
	v_pk_fma_f32 v[12:13], v[48:49], s[74:75], v[22:23] op_sel_hi:[1,0,1]
	v_cvt_pk_fp8_f32 v31, v28, v29
	v_cvt_pk_fp8_f32 v26, v8, v9
	v_cvt_pk_fp8_f32 v27, v12, v13
	v_pk_fma_f32 v[28:29], v[66:67], s[74:75], v[24:25] op_sel_hi:[1,0,1]
	v_pk_fma_f32 v[8:9], v[54:55], s[74:75], v[20:21] op_sel_hi:[1,0,1]
	v_pk_fma_f32 v[12:13], v[50:51], s[74:75], v[24:25] op_sel_hi:[1,0,1]
	v_cvt_pk_fp8_f32 v31, v28, v29 op_sel:[0,0,1]
	v_cvt_pk_fp8_f32 v26, v8, v9 op_sel:[0,0,1]
	v_cvt_pk_fp8_f32 v27, v12, v13 op_sel:[0,0,1]
	ds_bpermute_b32 v8, v169, v14
	ds_bpermute_b32 v9, v169, v15
	v_pk_fma_f32 v[14:15], v[44:45], s[74:75], v[18:19] op_sel_hi:[1,0,1]
	v_cvt_pk_fp8_f32 v28, v14, v15
	ds_bpermute_b32 v12, v169, v26
	ds_bpermute_b32 v13, v169, v27
	v_pk_fma_f32 v[26:27], v[40:41], s[74:75], v[22:23] op_sel_hi:[1,0,1]
	v_pk_fma_f32 v[14:15], v[46:47], s[74:75], v[20:21] op_sel_hi:[1,0,1]
	v_cvt_pk_fp8_f32 v29, v26, v27
	v_cvt_pk_fp8_f32 v28, v14, v15 op_sel:[0,0,1]
	v_pk_fma_f32 v[14:15], v[36:37], s[74:75], v[18:19] op_sel_hi:[1,0,1]
	v_pk_fma_f32 v[18:19], v[32:33], s[74:75], v[22:23] op_sel_hi:[1,0,1]
	v_cvt_pk_fp8_f32 v22, v14, v15
	v_cvt_pk_fp8_f32 v23, v18, v19
	v_pk_fma_f32 v[26:27], v[42:43], s[74:75], v[24:25] op_sel_hi:[1,0,1]
	v_pk_fma_f32 v[14:15], v[38:39], s[74:75], v[20:21] op_sel_hi:[1,0,1]
	v_cvt_pk_fp8_f32 v29, v26, v27 op_sel:[0,0,1]
	v_pk_fma_f32 v[18:19], v[34:35], s[74:75], v[24:25] op_sel_hi:[1,0,1]
	ds_bpermute_b32 v6, v169, v30
	ds_bpermute_b32 v7, v169, v31
	v_cvt_pk_fp8_f32 v22, v14, v15 op_sel:[0,0,1]
	v_cvt_pk_fp8_f32 v23, v18, v19 op_sel:[0,0,1]
	ds_bpermute_b32 v14, v169, v28
	ds_bpermute_b32 v15, v169, v29
	v_readlane_b32 s90, v255, 27
	ds_bpermute_b32 v18, v169, v22
	ds_bpermute_b32 v19, v169, v23
	s_and_b64 vcc, exec, s[20:21]
	v_mov_b32_e32 v170, v214
	v_mov_b32_e32 v166, v196
	v_mov_b32_e32 v174, v197
	v_mov_b32_e32 v168, v195
	s_mov_b32 s12, s81
	s_mov_b32 s14, s80
	s_mov_b64 s[24:25], s[16:17]
	s_mov_b64 s[22:23], s[18:19]
	s_mov_b32 s82, s73
	v_readlane_b32 s91, v255, 28
	v_readlane_b32 s73, v255, 29
	v_readlane_b32 s87, v255, 30
	v_readlane_b32 s85, v255, 31
	s_waitcnt lgkmcnt(0)
	global_store_dwordx2 v[0:1], v[6:7], off offset:128
	global_store_dwordx2 v[4:5], v[8:9], off offset:128
	global_store_dwordx2 v[10:11], v[12:13], off offset:128
	global_store_dwordx2 v[16:17], v[14:15], off offset:128
	global_store_dwordx2 v[2:3], v[18:19], off offset:128
	s_cbranch_vccnz .LBB0_1672
